# w2 conversion in the expert GEMM 1 epilogues, staggered: workgroups with bit 3 clear convert in rounds 0-7, the others in rounds 8-15
# speedup vs baseline: 1.0416x; 1.0028x over previous
.LBB0_1061:
	v_mov_b32_e32 v2, v243
	s_nop 15
	s_nop 15
	s_lshl_b32 s23, s51, 8
	v_readfirstlane_b32 s21, v2
	s_ashr_i32 s25, s21, 2
	s_andn2_b32 s25, s25, 63
	s_lshr_b32 s21, s21, 1
	s_add_i32 s25, s25, s23
	s_lshl_b32 s23, s76, 7
	s_and_b32 s21, s21, 0x60
	v_and_or_b32 v6, v2, 15, s25
	s_or_b32 s21, s21, s23
	v_lshrrev_b32_e32 v2, 1, v2
	v_and_or_b32 v4, v2, 24, s21
	s_waitcnt vmcnt(8)
	s_mov_b32 s32, 0
	s_cmp_gt_u32 s74, 2
	s_cbranch_scc1 .Lcg_skip_i
	v_readlane_b32 s84, v255, 7
	s_bfe_u32 s85, s84, 0x10003
	s_lshr_b32 s92, s51, 8
	s_cmp_lg_u32 s92, s85
	s_cbranch_scc1 .Lcg_skip_i
	s_load_dword s101, s[0:1], 0xb0
	s_load_dwordx2 s[80:81], s[0:1], 0x78
	s_load_dwordx2 s[82:83], s[0:1], 0xa0
	v_readfirstlane_b32 s85, v0
	s_lshr_b32 s85, s85, 6
	s_lshl_b32 s84, s84, 3
	s_add_i32 s84, s84, s85
	s_bfe_u32 s85, s51, 0x30005
	s_lshl_b32 s85, s85, 11
	s_add_i32 s85, s85, s84
	s_lshr_b32 s84, s85, 9
	s_add_i32 s92, s74, 1
	s_lshl_b32 s92, s92, 5
	s_add_i32 s84, s84, s92
	s_lshl_b32 s92, s84, 22
	s_bfe_u32 s93, s85, 0x30006
	s_lshl_b32 s93, s93, 19
	s_add_u32 s92, s92, s93
	s_and_b32 s93, s85, 63
	s_lshl_b32 s93, s93, 6
	s_add_u32 s100, s92, s93
	s_lshl_b32 s92, s84, 20
	s_and_b32 s93, s85, 63
	s_lshl_b32 s93, s93, 14
	s_add_u32 s92, s92, s93
	s_bfe_u32 s93, s85, 0x30006
	s_lshl_b32 s93, s93, 7
	s_add_u32 s92, s92, s93
	s_add_u32 s92, s92, 0x21f00000
	s_waitcnt lgkmcnt(0)
	s_cmpk_lg_i32 s101, 0x100
	s_cbranch_scc1 .Lcg_skip_i
	s_add_u32 s80, s80, s100
	s_addc_u32 s81, s81, 0
	s_add_u32 s82, s82, s92
	s_addc_u32 s83, s83, 0
	v_and_b32_e32 v56, 63, v0
	v_lshrrev_b32_e32 v57, 2, v56
	v_and_b32_e32 v56, 3, v56
	v_lshlrev_b32_e32 v57, 14, v57
	v_lshl_or_b32 v56, v56, 4, v57
	global_load_dwordx4 v[24:27], v56, s[80:81] nt
	v_add_u32_e32 v57, 0x1000, v56
	global_load_dwordx4 v[28:31], v57, s[80:81] nt
	v_add_u32_e32 v57, 0x2000, v56
	global_load_dwordx4 v[32:35], v57, s[80:81] nt
	v_add_u32_e32 v57, 0x3000, v56
	global_load_dwordx4 v[36:39], v57, s[80:81] nt
	v_add_u32_e32 v57, 0x40000, v56
	global_load_dwordx4 v[40:43], v57, s[80:81] nt
	v_add_u32_e32 v57, 0x41000, v56
	global_load_dwordx4 v[44:47], v57, s[80:81] nt
	v_add_u32_e32 v57, 0x42000, v56
	global_load_dwordx4 v[48:51], v57, s[80:81] nt
	v_add_u32_e32 v57, 0x43000, v56
	global_load_dwordx4 v[52:55], v57, s[80:81] nt
	s_mov_b32 s32, 1
